# P18 final combine: hand-written loop, two tokens per iteration with all 44 loads issued before the reductions; stacked on v022
# baseline (speedup 1.0000x reference)
.LBB0_3225:
	s_or_b64 exec, exec, s[0:1]
	v_readlane_b32 s1, v252, 48
	s_abs_i32 s0, s1
	v_cvt_f32_u32_e32 v0, s0
	s_sub_i32 s2, 0, s0
	s_ashr_i32 s1, s1, 31
	s_waitcnt lgkmcnt(0)
	v_rcp_iflag_f32_e32 v0, v0
	s_barrier
	v_mul_f32_e32 v0, 0x4f7ffffe, v0
	v_cvt_u32_f32_e32 v0, v0
	s_nop 0
	v_readfirstlane_b32 s3, v0
	s_mul_i32 s2, s2, s3
	s_mul_hi_u32 s2, s3, s2
	s_add_i32 s3, s3, s2
	s_lshr_b32 s2, s3, 16
	s_mul_i32 s3, s2, s0
	s_sub_i32 s3, 0x10000, s3
	s_add_i32 s4, s2, 1
	s_sub_i32 s5, s3, s0
	s_cmp_ge_u32 s3, s0
	s_cselect_b32 s2, s4, s2
	s_cselect_b32 s3, s5, s3
	s_add_i32 s4, s2, 1
	s_cmp_ge_u32 s3, s0
	s_cselect_b32 s0, s4, s2
	s_xor_b32 s0, s0, s1
	s_sub_i32 s0, s0, s1
	s_cmp_lt_i32 s0, 1
	s_cbranch_scc1 .LBB0_3232
	v_readlane_b32 s1, v252, 47
	s_mul_i32 s2, s0, s1
	s_ashr_i32 s1, s2, 11
	s_mul_hi_i32 s3, s1, 0x6000
	s_mulk_i32 s1, 0x6000
	v_readlane_b32 s4, v253, 7
	s_add_u32 s4, s4, s1
	v_readlane_b32 s1, v253, 8
	s_addc_u32 s5, s1, s3
	v_mov_b32_e32 v17, 0
	v_lshlrev_b32_e32 v16, 4, v174
	v_lshl_add_u64 v[8:9], s[4:5], 0, v[16:17]
	s_mov_b64 s[4:5], 0x5000
	v_add_co_u32_e32 v20, vcc, 0x5000, v8
	v_lshl_add_u64 v[18:19], v[8:9], 0, s[4:5]
	s_nop 0
	v_addc_co_u32_e32 v21, vcc, 0, v9, vcc
	global_load_dwordx4 v[0:3], v[18:19], off offset:1024
	global_load_dwordx4 v[4:7], v[18:19], off offset:2048
	global_load_dwordx4 v[8:11], v[20:21], off
	global_load_dwordx4 v[12:15], v[18:19], off offset:3072
	v_readlane_b32 s20, v252, 0
	s_add_i32 s12, s2, s0
	v_readlane_b32 s26, v252, 6
	v_readlane_b32 s27, v252, 7
	s_cmp_lg_u64 s[26:27], 0
	s_cselect_b64 s[0:1], -1, 0
	s_lshl_b32 s8, s2, 2
	s_ashr_i32 s3, s2, 31
	v_cndmask_b32_e64 v39, 0, 1, s[0:1]
	s_or_b32 s8, s8, 3
	s_lshl_b64 s[0:1], s[2:3], 11
	v_readlane_b32 s22, v252, 2
	v_readlane_b32 s23, v252, 3
	s_add_u32 s0, s70, s0
	v_lshlrev_b32_e32 v18, 3, v174
	v_mov_b32_e32 v19, v17
	s_mov_b64 s[22:23], s[26:27]
	s_addc_u32 s1, s71, s1
	s_lshl_b64 s[18:19], s[2:3], 12
	v_lshl_add_u64 v[18:19], s[0:1], 0, v[18:19]
	s_add_u32 s0, s22, s18
	s_addc_u32 s1, s23, s19
	s_mov_b32 s10, 0x3e800000
	s_mov_b64 s[14:15], 0x6d400000
	s_mov_b64 s[16:17], 0xc00
	v_lshl_add_u64 v[20:21], s[0:1], 0, v[16:17]
	v_lshlrev_b32_e32 v38, 2, v174
	s_mov_b64 s[4:5], 0x800
	s_mov_b64 s[6:7], 0x1000
	v_lshl_add_u64 v[18:19], v[18:19], 0, s[14:15]
	s_add_i32 s3, 0, 0x20480
	v_lshl_add_u64 v[20:21], v[20:21], 0, s[16:17]
	v_cmp_ne_u32_e64 s[0:1], 1, v39
	v_readlane_b32 s21, v252, 1
	v_readlane_b32 s24, v252, 4
	v_readlane_b32 s25, v252, 5
	s_waitcnt vmcnt(3)
	v_pk_mul_f32 v[22:23], v[2:3], s[10:11] op_sel_hi:[1,0]
	v_pk_mul_f32 v[24:25], v[0:1], s[10:11] op_sel_hi:[1,0]
	s_waitcnt vmcnt(2)
	v_pk_mul_f32 v[26:27], v[6:7], s[10:11] op_sel_hi:[1,0]
	v_pk_mul_f32 v[28:29], v[4:5], s[10:11] op_sel_hi:[1,0]
	s_waitcnt vmcnt(1)
	v_pk_mul_f32 v[30:31], v[10:11], s[10:11] op_sel_hi:[1,0]
	v_pk_mul_f32 v[32:33], v[8:9], s[10:11] op_sel_hi:[1,0]
	s_waitcnt vmcnt(0)
	v_pk_mul_f32 v[34:35], v[14:15], s[10:11] op_sel_hi:[1,0]
	v_pk_mul_f32 v[36:37], v[12:13], s[10:11] op_sel_hi:[1,0]
	s_and_b64 vcc, exec, s[0:1]
	s_cbranch_vccnz .LBB0_3228
	s_sub_i32 s10, s12, s2
	s_bitcmp1_b32 s10, 0
	s_cbranch_scc1 .LBB0_3228
.Lp18_loop:
	s_add_i32 s10, s8, -3
	s_ashr_i32 s11, s10, 31
	s_lshl_b64 s[10:11], s[10:11], 2
	s_add_u32 s14, s74, s10
	s_addc_u32 s15, s75, s11
	s_add_u32 s10, s76, s10
	s_addc_u32 s11, s77, s11
	global_load_dwordx4 v[100:103], v17, s[14:15]
	global_load_dwordx4 v[104:107], v17, s[10:11]
	s_add_i32 s10, s8, 1
	s_ashr_i32 s11, s10, 31
	s_lshl_b64 s[10:11], s[10:11], 2
	s_add_u32 s14, s74, s10
	s_addc_u32 s15, s75, s11
	s_add_u32 s10, s76, s10
	s_addc_u32 s11, s77, s11
	global_load_dwordx4 v[108:111], v17, s[14:15]
	global_load_dwordx4 v[112:115], v17, s[10:11]
	global_load_dwordx2 v[8:9], v[18:19], off
	global_load_dwordx2 v[10:11], v[18:19], off offset:512
	global_load_dwordx2 v[12:13], v[18:19], off offset:1024
	global_load_dwordx2 v[14:15], v[18:19], off offset:1536
	v_lshl_add_u64 v[172:173], v[18:19], 0, s[4:5]
	global_load_dwordx2 v[88:89], v[172:173], off
	global_load_dwordx2 v[90:91], v[172:173], off offset:512
	global_load_dwordx2 v[92:93], v[172:173], off offset:1024
	global_load_dwordx2 v[94:95], v[172:173], off offset:1536
	s_waitcnt vmcnt(10)
	v_lshlrev_b32_e32 v97, 2, v100
	v_add_u32_e32 v97, s3, v97
	ds_read_b32 v98, v97
	v_mov_b32_e32 v160, v104
	v_ashrrev_i32_e32 v161, 31, v160
	v_lshlrev_b64 v[116:117], 10, v[160:161]
	s_waitcnt lgkmcnt(0)
	v_ashrrev_i32_e32 v99, 31, v98
	v_lshlrev_b64 v[162:163], 18, v[98:99]
	v_lshl_add_u64 v[162:163], s[92:93], 0, v[162:163]
	v_lshl_add_u64 v[162:163], v[162:163], 0, v[116:117]
	s_nop 0
	v_readfirstlane_b32 s10, v162
	v_readfirstlane_b32 s11, v163
	s_nop 4
	global_load_dword v16, v38, s[10:11]
	global_load_dword v39, v38, s[10:11] offset:256
	global_load_dword v50, v38, s[10:11] offset:512
	global_load_dword v54, v38, s[10:11] offset:768
	v_lshlrev_b32_e32 v97, 2, v101
	v_add_u32_e32 v97, s3, v97
	ds_read_b32 v98, v97
	v_mov_b32_e32 v160, v105
	v_ashrrev_i32_e32 v161, 31, v160
	v_lshlrev_b64 v[116:117], 10, v[160:161]
	s_waitcnt lgkmcnt(0)
	v_ashrrev_i32_e32 v99, 31, v98
	v_lshlrev_b64 v[162:163], 18, v[98:99]
	v_lshl_add_u64 v[162:163], s[92:93], 0, v[162:163]
	v_lshl_add_u64 v[162:163], v[162:163], 0, v[116:117]
	s_nop 0
	v_readfirstlane_b32 s10, v162
	v_readfirstlane_b32 s11, v163
	s_nop 4
	global_load_dword v58, v38, s[10:11]
	global_load_dword v62, v38, s[10:11] offset:256
	global_load_dword v66, v38, s[10:11] offset:512
	global_load_dword v70, v38, s[10:11] offset:768
	v_lshlrev_b32_e32 v97, 2, v102
	v_add_u32_e32 v97, s3, v97
	ds_read_b32 v98, v97
	v_mov_b32_e32 v160, v106
	v_ashrrev_i32_e32 v161, 31, v160
	v_lshlrev_b64 v[116:117], 10, v[160:161]
	s_waitcnt lgkmcnt(0)
	v_ashrrev_i32_e32 v99, 31, v98
	v_lshlrev_b64 v[162:163], 18, v[98:99]
	v_lshl_add_u64 v[162:163], s[92:93], 0, v[162:163]
	v_lshl_add_u64 v[162:163], v[162:163], 0, v[116:117]
	s_nop 0
	v_readfirstlane_b32 s10, v162
	v_readfirstlane_b32 s11, v163
	s_nop 4
	global_load_dword v72, v38, s[10:11]
	global_load_dword v73, v38, s[10:11] offset:256
	global_load_dword v74, v38, s[10:11] offset:512
	global_load_dword v75, v38, s[10:11] offset:768
	v_lshlrev_b32_e32 v97, 2, v103
	v_add_u32_e32 v97, s3, v97
	ds_read_b32 v98, v97
	v_mov_b32_e32 v160, v107
	v_ashrrev_i32_e32 v161, 31, v160
	v_lshlrev_b64 v[116:117], 10, v[160:161]
	s_waitcnt lgkmcnt(0)
	v_ashrrev_i32_e32 v99, 31, v98
	v_lshlrev_b64 v[162:163], 18, v[98:99]
	v_lshl_add_u64 v[162:163], s[92:93], 0, v[162:163]
	v_lshl_add_u64 v[162:163], v[162:163], 0, v[116:117]
	s_nop 0
	v_readfirstlane_b32 s10, v162
	v_readfirstlane_b32 s11, v163
	s_nop 4
	global_load_dword v76, v38, s[10:11]
	global_load_dword v77, v38, s[10:11] offset:256
	global_load_dword v78, v38, s[10:11] offset:512
	global_load_dword v79, v38, s[10:11] offset:768
	s_waitcnt vmcnt(24)
	v_lshlrev_b32_e32 v97, 2, v108
	v_add_u32_e32 v97, s3, v97
	ds_read_b32 v98, v97
	v_mov_b32_e32 v160, v112
	v_ashrrev_i32_e32 v161, 31, v160
	v_lshlrev_b64 v[116:117], 10, v[160:161]
	s_waitcnt lgkmcnt(0)
	v_ashrrev_i32_e32 v99, 31, v98
	v_lshlrev_b64 v[162:163], 18, v[98:99]
	v_lshl_add_u64 v[162:163], s[92:93], 0, v[162:163]
	v_lshl_add_u64 v[162:163], v[162:163], 0, v[116:117]
	s_nop 0
	v_readfirstlane_b32 s10, v162
	v_readfirstlane_b32 s11, v163
	s_nop 4
	global_load_dword v96, v38, s[10:11]
	global_load_dword v119, v38, s[10:11] offset:256
	global_load_dword v130, v38, s[10:11] offset:512
	global_load_dword v134, v38, s[10:11] offset:768
	v_lshlrev_b32_e32 v97, 2, v109
	v_add_u32_e32 v97, s3, v97
	ds_read_b32 v98, v97
	v_mov_b32_e32 v160, v113
	v_ashrrev_i32_e32 v161, 31, v160
	v_lshlrev_b64 v[116:117], 10, v[160:161]
	s_waitcnt lgkmcnt(0)
	v_ashrrev_i32_e32 v99, 31, v98
	v_lshlrev_b64 v[162:163], 18, v[98:99]
	v_lshl_add_u64 v[162:163], s[92:93], 0, v[162:163]
	v_lshl_add_u64 v[162:163], v[162:163], 0, v[116:117]
	s_nop 0
	v_readfirstlane_b32 s10, v162
	v_readfirstlane_b32 s11, v163
	s_nop 4
	global_load_dword v138, v38, s[10:11]
	global_load_dword v142, v38, s[10:11] offset:256
	global_load_dword v146, v38, s[10:11] offset:512
	global_load_dword v150, v38, s[10:11] offset:768
	v_lshlrev_b32_e32 v97, 2, v110
	v_add_u32_e32 v97, s3, v97
	ds_read_b32 v98, v97
	v_mov_b32_e32 v160, v114
	v_ashrrev_i32_e32 v161, 31, v160
	v_lshlrev_b64 v[116:117], 10, v[160:161]
	s_waitcnt lgkmcnt(0)
	v_ashrrev_i32_e32 v99, 31, v98
	v_lshlrev_b64 v[162:163], 18, v[98:99]
	v_lshl_add_u64 v[162:163], s[92:93], 0, v[162:163]
	v_lshl_add_u64 v[162:163], v[162:163], 0, v[116:117]
	s_nop 0
	v_readfirstlane_b32 s10, v162
	v_readfirstlane_b32 s11, v163
	s_nop 4
	global_load_dword v152, v38, s[10:11]
	global_load_dword v153, v38, s[10:11] offset:256
	global_load_dword v154, v38, s[10:11] offset:512
	global_load_dword v155, v38, s[10:11] offset:768
	v_lshlrev_b32_e32 v97, 2, v111
	v_add_u32_e32 v97, s3, v97
	ds_read_b32 v98, v97
	v_mov_b32_e32 v160, v115
	v_ashrrev_i32_e32 v161, 31, v160
	v_lshlrev_b64 v[116:117], 10, v[160:161]
	s_waitcnt lgkmcnt(0)
	v_ashrrev_i32_e32 v99, 31, v98
	v_lshlrev_b64 v[162:163], 18, v[98:99]
	v_lshl_add_u64 v[162:163], s[92:93], 0, v[162:163]
	v_lshl_add_u64 v[162:163], v[162:163], 0, v[116:117]
	s_nop 0
	v_readfirstlane_b32 s10, v162
	v_readfirstlane_b32 s11, v163
	s_nop 4
	global_load_dword v156, v38, s[10:11]
	global_load_dword v157, v38, s[10:11] offset:256
	global_load_dword v158, v38, s[10:11] offset:512
	global_load_dword v159, v38, s[10:11] offset:768
	s_waitcnt vmcnt(16)
	v_lshlrev_b32_e32 v2, 16, v9
	v_lshlrev_b32_e32 v0, 16, v8
	v_and_b32_e32 v1, 0xffff0000, v8
	v_and_b32_e32 v3, 0xffff0000, v9
	v_lshlrev_b32_e32 v4, 16, v10
	v_and_b32_e32 v5, 0xffff0000, v10
	v_lshlrev_b32_e32 v6, 16, v11
	v_and_b32_e32 v7, 0xffff0000, v11
	v_lshlrev_b32_e32 v40, 16, v12
	v_and_b32_e32 v41, 0xffff0000, v12
	v_lshlrev_b32_e32 v42, 16, v13
	v_and_b32_e32 v43, 0xffff0000, v13
	v_lshlrev_b32_e32 v44, 16, v14
	v_and_b32_e32 v45, 0xffff0000, v14
	v_lshlrev_b32_e32 v46, 16, v15
	v_and_b32_e32 v47, 0xffff0000, v15
	v_cvt_pk_f32_fp8_e32 v[8:9], v16
	v_cvt_pk_f32_fp8_sdwa v[10:11], v16 src0_sel:WORD_1
	v_cvt_pk_f32_fp8_e32 v[12:13], v39
	v_cvt_pk_f32_fp8_sdwa v[14:15], v39 src0_sel:WORD_1
	v_pk_add_f32 v[8:9], v[8:9], 0 op_sel_hi:[1,0]
	v_pk_add_f32 v[10:11], v[10:11], 0 op_sel_hi:[1,0]
	v_pk_add_f32 v[12:13], v[12:13], 0 op_sel_hi:[1,0]
	v_cvt_pk_f32_fp8_e32 v[48:49], v50
	v_cvt_pk_f32_fp8_sdwa v[50:51], v50 src0_sel:WORD_1
	v_cvt_pk_f32_fp8_e32 v[52:53], v54
	v_cvt_pk_f32_fp8_sdwa v[54:55], v54 src0_sel:WORD_1
	v_pk_add_f32 v[14:15], v[14:15], 0 op_sel_hi:[1,0]
	v_cvt_pk_f32_fp8_e32 v[56:57], v58
	v_cvt_pk_f32_fp8_sdwa v[58:59], v58 src0_sel:WORD_1
	v_cvt_pk_f32_fp8_e32 v[60:61], v62
	v_cvt_pk_f32_fp8_sdwa v[62:63], v62 src0_sel:WORD_1
	v_pk_add_f32 v[50:51], v[50:51], 0 op_sel_hi:[1,0]
	v_cvt_pk_f32_fp8_e32 v[64:65], v66
	v_cvt_pk_f32_fp8_sdwa v[66:67], v66 src0_sel:WORD_1
	v_cvt_pk_f32_fp8_e32 v[68:69], v70
	v_cvt_pk_f32_fp8_sdwa v[70:71], v70 src0_sel:WORD_1
	v_pk_add_f32 v[48:49], v[48:49], 0 op_sel_hi:[1,0]
	v_pk_add_f32 v[54:55], v[54:55], 0 op_sel_hi:[1,0]
	v_pk_add_f32 v[52:53], v[52:53], 0 op_sel_hi:[1,0]
	v_pk_add_f32 v[8:9], v[8:9], v[56:57]
	v_pk_add_f32 v[10:11], v[10:11], v[58:59]
	v_pk_add_f32 v[12:13], v[12:13], v[60:61]
	v_pk_add_f32 v[14:15], v[14:15], v[62:63]
	v_pk_add_f32 v[48:49], v[48:49], v[64:65]
	v_pk_add_f32 v[50:51], v[50:51], v[66:67]
	v_pk_add_f32 v[52:53], v[52:53], v[68:69]
	v_pk_add_f32 v[54:55], v[54:55], v[70:71]
	v_cvt_pk_f32_fp8_e32 v[56:57], v72
	v_cvt_pk_f32_fp8_sdwa v[58:59], v72 src0_sel:WORD_1
	v_cvt_pk_f32_fp8_e32 v[60:61], v73
	v_cvt_pk_f32_fp8_sdwa v[62:63], v73 src0_sel:WORD_1
	v_cvt_pk_f32_fp8_e32 v[64:65], v74
	v_cvt_pk_f32_fp8_sdwa v[66:67], v74 src0_sel:WORD_1
	v_cvt_pk_f32_fp8_e32 v[68:69], v75
	v_cvt_pk_f32_fp8_sdwa v[70:71], v75 src0_sel:WORD_1
	v_pk_add_f32 v[10:11], v[10:11], v[58:59]
	v_pk_add_f32 v[8:9], v[8:9], v[56:57]
	v_pk_add_f32 v[14:15], v[14:15], v[62:63]
	v_pk_add_f32 v[12:13], v[12:13], v[60:61]
	v_pk_add_f32 v[50:51], v[50:51], v[66:67]
	v_pk_add_f32 v[48:49], v[48:49], v[64:65]
	v_pk_add_f32 v[54:55], v[54:55], v[70:71]
	v_pk_add_f32 v[52:53], v[52:53], v[68:69]
	v_cvt_pk_f32_fp8_e32 v[56:57], v76
	v_cvt_pk_f32_fp8_sdwa v[58:59], v76 src0_sel:WORD_1
	v_cvt_pk_f32_fp8_e32 v[60:61], v77
	v_cvt_pk_f32_fp8_sdwa v[62:63], v77 src0_sel:WORD_1
	v_cvt_pk_f32_fp8_e32 v[64:65], v78
	v_cvt_pk_f32_fp8_sdwa v[66:67], v78 src0_sel:WORD_1
	v_cvt_pk_f32_fp8_e32 v[68:69], v79
	v_cvt_pk_f32_fp8_sdwa v[70:71], v79 src0_sel:WORD_1
	v_pk_add_f32 v[8:9], v[8:9], v[56:57]
	v_pk_add_f32 v[10:11], v[10:11], v[58:59]
	v_pk_add_f32 v[56:57], v[12:13], v[60:61]
	v_pk_add_f32 v[58:59], v[14:15], v[62:63]
	v_pk_add_f32 v[48:49], v[48:49], v[64:65]
	v_pk_add_f32 v[50:51], v[50:51], v[66:67]
	v_pk_add_f32 v[52:53], v[52:53], v[68:69]
	v_pk_add_f32 v[54:55], v[54:55], v[70:71]
	v_pk_fma_f32 v[14:15], v[30:31], v[10:11], v[2:3]
	v_pk_fma_f32 v[12:13], v[32:33], v[8:9], v[0:1]
	v_pk_fma_f32 v[10:11], v[22:23], v[58:59], v[6:7]
	v_pk_fma_f32 v[8:9], v[24:25], v[56:57], v[4:5]
	v_pk_fma_f32 v[6:7], v[26:27], v[50:51], v[42:43]
	v_pk_fma_f32 v[4:5], v[28:29], v[48:49], v[40:41]
	v_pk_fma_f32 v[2:3], v[34:35], v[54:55], v[46:47]
	v_pk_fma_f32 v[0:1], v[36:37], v[52:53], v[44:45]
	global_store_dwordx4 v[20:21], v[12:15], off offset:-3072
	global_store_dwordx4 v[20:21], v[8:11], off offset:-2048
	global_store_dwordx4 v[20:21], v[4:7], off offset:-1024
	global_store_dwordx4 v[20:21], v[0:3], off
	v_lshl_add_u64 v[172:173], v[20:21], 0, s[6:7]
	s_waitcnt vmcnt(4)
	v_lshlrev_b32_e32 v82, 16, v89
	v_lshlrev_b32_e32 v80, 16, v88
	v_and_b32_e32 v81, 0xffff0000, v88
	v_and_b32_e32 v83, 0xffff0000, v89
	v_lshlrev_b32_e32 v84, 16, v90
	v_and_b32_e32 v85, 0xffff0000, v90
	v_lshlrev_b32_e32 v86, 16, v91
	v_and_b32_e32 v87, 0xffff0000, v91
	v_lshlrev_b32_e32 v120, 16, v92
	v_and_b32_e32 v121, 0xffff0000, v92
	v_lshlrev_b32_e32 v122, 16, v93
	v_and_b32_e32 v123, 0xffff0000, v93
	v_lshlrev_b32_e32 v124, 16, v94
	v_and_b32_e32 v125, 0xffff0000, v94
	v_lshlrev_b32_e32 v126, 16, v95
	v_and_b32_e32 v127, 0xffff0000, v95
	v_cvt_pk_f32_fp8_e32 v[88:89], v96
	v_cvt_pk_f32_fp8_sdwa v[90:91], v96 src0_sel:WORD_1
	v_cvt_pk_f32_fp8_e32 v[92:93], v119
	v_cvt_pk_f32_fp8_sdwa v[94:95], v119 src0_sel:WORD_1
	v_pk_add_f32 v[88:89], v[88:89], 0 op_sel_hi:[1,0]
	v_pk_add_f32 v[90:91], v[90:91], 0 op_sel_hi:[1,0]
	v_pk_add_f32 v[92:93], v[92:93], 0 op_sel_hi:[1,0]
	v_cvt_pk_f32_fp8_e32 v[128:129], v130
	v_cvt_pk_f32_fp8_sdwa v[130:131], v130 src0_sel:WORD_1
	v_cvt_pk_f32_fp8_e32 v[132:133], v134
	v_cvt_pk_f32_fp8_sdwa v[134:135], v134 src0_sel:WORD_1
	v_pk_add_f32 v[94:95], v[94:95], 0 op_sel_hi:[1,0]
	v_cvt_pk_f32_fp8_e32 v[136:137], v138
	v_cvt_pk_f32_fp8_sdwa v[138:139], v138 src0_sel:WORD_1
	v_cvt_pk_f32_fp8_e32 v[140:141], v142
	v_cvt_pk_f32_fp8_sdwa v[142:143], v142 src0_sel:WORD_1
	v_pk_add_f32 v[130:131], v[130:131], 0 op_sel_hi:[1,0]
	v_cvt_pk_f32_fp8_e32 v[144:145], v146
	v_cvt_pk_f32_fp8_sdwa v[146:147], v146 src0_sel:WORD_1
	v_cvt_pk_f32_fp8_e32 v[148:149], v150
	v_cvt_pk_f32_fp8_sdwa v[150:151], v150 src0_sel:WORD_1
	v_pk_add_f32 v[128:129], v[128:129], 0 op_sel_hi:[1,0]
	v_pk_add_f32 v[134:135], v[134:135], 0 op_sel_hi:[1,0]
	v_pk_add_f32 v[132:133], v[132:133], 0 op_sel_hi:[1,0]
	v_pk_add_f32 v[88:89], v[88:89], v[136:137]
	v_pk_add_f32 v[90:91], v[90:91], v[138:139]
	v_pk_add_f32 v[92:93], v[92:93], v[140:141]
	v_pk_add_f32 v[94:95], v[94:95], v[142:143]
	v_pk_add_f32 v[128:129], v[128:129], v[144:145]
	v_pk_add_f32 v[130:131], v[130:131], v[146:147]
	v_pk_add_f32 v[132:133], v[132:133], v[148:149]
	v_pk_add_f32 v[134:135], v[134:135], v[150:151]
	v_cvt_pk_f32_fp8_e32 v[136:137], v152
	v_cvt_pk_f32_fp8_sdwa v[138:139], v152 src0_sel:WORD_1
	v_cvt_pk_f32_fp8_e32 v[140:141], v153
	v_cvt_pk_f32_fp8_sdwa v[142:143], v153 src0_sel:WORD_1
	v_cvt_pk_f32_fp8_e32 v[144:145], v154
	v_cvt_pk_f32_fp8_sdwa v[146:147], v154 src0_sel:WORD_1
	v_cvt_pk_f32_fp8_e32 v[148:149], v155
	v_cvt_pk_f32_fp8_sdwa v[150:151], v155 src0_sel:WORD_1
	v_pk_add_f32 v[90:91], v[90:91], v[138:139]
	v_pk_add_f32 v[88:89], v[88:89], v[136:137]
	v_pk_add_f32 v[94:95], v[94:95], v[142:143]
	v_pk_add_f32 v[92:93], v[92:93], v[140:141]
	v_pk_add_f32 v[130:131], v[130:131], v[146:147]
	v_pk_add_f32 v[128:129], v[128:129], v[144:145]
	v_pk_add_f32 v[134:135], v[134:135], v[150:151]
	v_pk_add_f32 v[132:133], v[132:133], v[148:149]
	v_cvt_pk_f32_fp8_e32 v[136:137], v156
	v_cvt_pk_f32_fp8_sdwa v[138:139], v156 src0_sel:WORD_1
	v_cvt_pk_f32_fp8_e32 v[140:141], v157
	v_cvt_pk_f32_fp8_sdwa v[142:143], v157 src0_sel:WORD_1
	v_cvt_pk_f32_fp8_e32 v[144:145], v158
	v_cvt_pk_f32_fp8_sdwa v[146:147], v158 src0_sel:WORD_1
	v_cvt_pk_f32_fp8_e32 v[148:149], v159
	v_cvt_pk_f32_fp8_sdwa v[150:151], v159 src0_sel:WORD_1
	v_pk_add_f32 v[88:89], v[88:89], v[136:137]
	v_pk_add_f32 v[90:91], v[90:91], v[138:139]
	v_pk_add_f32 v[136:137], v[92:93], v[140:141]
	v_pk_add_f32 v[138:139], v[94:95], v[142:143]
	v_pk_add_f32 v[128:129], v[128:129], v[144:145]
	v_pk_add_f32 v[130:131], v[130:131], v[146:147]
	v_pk_add_f32 v[132:133], v[132:133], v[148:149]
	v_pk_add_f32 v[134:135], v[134:135], v[150:151]
	v_pk_fma_f32 v[94:95], v[30:31], v[90:91], v[82:83]
	v_pk_fma_f32 v[92:93], v[32:33], v[88:89], v[80:81]
	v_pk_fma_f32 v[90:91], v[22:23], v[138:139], v[86:87]
	v_pk_fma_f32 v[88:89], v[24:25], v[136:137], v[84:85]
	v_pk_fma_f32 v[86:87], v[26:27], v[130:131], v[122:123]
	v_pk_fma_f32 v[84:85], v[28:29], v[128:129], v[120:121]
	v_pk_fma_f32 v[82:83], v[34:35], v[134:135], v[126:127]
	v_pk_fma_f32 v[80:81], v[36:37], v[132:133], v[124:125]
	global_store_dwordx4 v[172:173], v[92:95], off offset:-3072
	global_store_dwordx4 v[172:173], v[88:91], off offset:-2048
	global_store_dwordx4 v[172:173], v[84:87], off offset:-1024
	global_store_dwordx4 v[172:173], v[80:83], off
	s_add_i32 s2, s2, 2
	s_add_i32 s8, s8, 8
	v_lshl_add_u64 v[18:19], v[18:19], 0, s[6:7]
	v_lshl_add_u64 v[20:21], v[172:173], 0, s[6:7]
	s_cmp_lt_i32 s2, s12
	s_cbranch_scc1 .Lp18_loop
	s_branch .LBB0_3232
